# speedup vs baseline: 1.0002x; 1.0002x over previous
.Lu0_1:
	ds_read_b64_tr_b16 v[178:179], v206 offset:24576
	ds_read_b64_tr_b16 v[180:181], v206 offset:25600
	s_waitcnt lgkmcnt(9)
	v_mfma_f32_32x32x16_f16 v[98:113], v[82:85], v[154:157], v[34:49]
	v_cvt_pk_f16_f32 v158, v66, v67
	v_cvt_pk_f16_f32 v159, v68, v69
	v_add_f32_e32 v224, v66, v70
	v_add_f32_e32 v225, v67, v71
	v_add_f32_e32 v226, v68, v72
	v_add_f32_e32 v227, v69, v73
	ds_read_b64_tr_b16 v[174:175], v207 offset:24576
	ds_read_b64_tr_b16 v[176:177], v207 offset:25600
	s_waitcnt lgkmcnt(10)
	v_mfma_f32_32x32x16_f16 v[82:97], v[170:173], v[154:157], v[34:49]
	v_cvt_pk_f16_f32 v160, v70, v71
	v_cvt_pk_f16_f32 v161, v72, v73
	v_add_f32_e32 v224, v74, v224
	v_add_f32_e32 v225, v75, v225
	v_add_f32_e32 v226, v76, v226
	v_add_f32_e32 v227, v77, v227
	ds_read_b64_tr_b16 v[170:171], v206 offset:26624
	ds_read_b64_tr_b16 v[172:173], v206 offset:27648
	s_waitcnt lgkmcnt(11)
	v_mfma_f32_32x32x16_f16 v[98:113], v[166:169], v[146:149], v[98:113]
	v_cvt_pk_f16_f32 v150, v74, v75
	v_cvt_pk_f16_f32 v151, v76, v77
	v_add_f32_e32 v224, v78, v224
	v_add_f32_e32 v225, v79, v225
	v_add_f32_e32 v226, v80, v226
	v_add_f32_e32 v227, v81, v227
	ds_read_b64_tr_b16 v[74:75], v207 offset:26624
	ds_read_b64_tr_b16 v[76:77], v207 offset:27648
	s_waitcnt lgkmcnt(12)
	v_mfma_f32_32x32x16_f16 v[82:97], v[162:165], v[146:149], v[82:97]
	v_cvt_pk_f16_f32 v152, v78, v79
	v_cvt_pk_f16_f32 v153, v80, v81
	v_add_f32_e32 v224, v50, v224
	v_add_f32_e32 v225, v51, v225
	v_add_f32_e32 v226, v52, v226
	v_add_f32_e32 v227, v53, v227
	ds_read_b64_tr_b16 v[70:71], v206 offset:28672
	ds_read_b64_tr_b16 v[72:73], v206 offset:29696
	s_waitcnt lgkmcnt(13)
	v_mfma_f32_32x32x16_f16 v[98:113], v[126:129], v[138:141], v[98:113]
	v_cvt_pk_f16_f32 v142, v50, v51
	v_cvt_pk_f16_f32 v143, v52, v53
	v_add_f32_e32 v224, v54, v224
	v_add_f32_e32 v225, v55, v225
	v_add_f32_e32 v226, v56, v226
	v_add_f32_e32 v227, v57, v227
	ds_read_b64_tr_b16 v[66:67], v207 offset:28672
	ds_read_b64_tr_b16 v[68:69], v207 offset:29696
	s_waitcnt lgkmcnt(14)
	v_mfma_f32_32x32x16_f16 v[82:97], v[122:125], v[138:141], v[82:97]
	v_cvt_pk_f16_f32 v144, v54, v55
	v_cvt_pk_f16_f32 v145, v56, v57
	v_add_f32_e32 v224, v58, v224
	v_add_f32_e32 v225, v59, v225
	v_add_f32_e32 v226, v60, v226
	v_add_f32_e32 v227, v61, v227
	ds_read_b64_tr_b16 v[54:55], v206 offset:30720
	ds_read_b64_tr_b16 v[56:57], v206 offset:31744
	s_waitcnt lgkmcnt(14)
	v_mfma_f32_32x32x16_f16 v[98:113], v[118:121], v[134:137], v[98:113]
	v_cvt_pk_f16_f32 v130, v58, v59
	v_cvt_pk_f16_f32 v131, v60, v61
	v_add_f32_e32 v224, v62, v224
	v_add_f32_e32 v225, v63, v225
	v_add_f32_e32 v226, v64, v226
	v_add_f32_e32 v227, v65, v227
	ds_read_b64_tr_b16 v[50:51], v207 offset:30720
	ds_read_b64_tr_b16 v[52:53], v207 offset:31744
	v_mfma_f32_32x32x16_f16 v[82:97], v[114:117], v[134:137], v[82:97]
	v_cvt_pk_f16_f32 v132, v62, v63
	v_cvt_pk_f16_f32 v133, v64, v65
	v_add_f32_e32 v224, v224, v225
	v_add_f32_e32 v226, v226, v227
	v_add_f32_e32 v60, v224, v226
	s_setprio 1
	s_add_i32 s26, s42, s36
	s_mov_b32 m0, s26
	s_nop 0
	global_load_lds_dwordx4 v221, s[50:51]
	s_add_i32 s26, s39, s35
	s_mov_b32 m0, s26
	s_nop 0
	global_load_lds_dwordx4 v222, s[52:53]
	v_max_f32_e32 v58, v98, v99
	v_max3_f32 v59, v100, v101, v83
	v_max3_f32 v58, v58, v82, v84
	v_max3_f32 v58, v58, v85, v102
	v_max3_f32 v59, v59, v104, v105
	v_max3_f32 v58, v58, v103, v86
	v_max3_f32 v59, v59, v88, v89
	v_max3_f32 v58, v58, v87, v106
	v_max3_f32 v59, v59, v108, v109
	v_max3_f32 v58, v58, v107, v90
	v_max3_f32 v59, v59, v92, v93
	v_max3_f32 v58, v58, v91, v110
	v_max3_f32 v59, v59, v112, v113
	v_max3_f32 v58, v58, v111, v94
	v_max3_f32 v59, v59, v96, v97
	v_max3_f32 v58, v58, v95, v59
	v_add_f32_e32 v198, v183, v60
	v_cmp_lt_f32_e32 vcc, s41, v58
	s_cmp_lg_u64 vcc, 0
	s_cselect_b64 s[26:27], -1, 0
	s_cbranch_vccnz .Lu0_9

.Lu0_4:
	s_add_i32 s26, s39, 0x2000
	s_cmpk_lg_i32 s39, 0x4000
	s_cselect_b32 s43, s26, 0
	ds_read_b64_tr_b16 v[126:127], v206 offset:32768
	ds_read_b64_tr_b16 v[128:129], v206 offset:33792
	s_waitcnt lgkmcnt(9)
	v_mfma_f32_32x32x16_f16 v[66:81], v[58:61], v[154:157], v[34:49]
	v_cvt_pk_f16_f32 v158, v98, v99
	v_cvt_pk_f16_f32 v159, v100, v101
	v_add_f32_e32 v224, v98, v102
	v_add_f32_e32 v225, v99, v103
	v_add_f32_e32 v226, v100, v104
	v_add_f32_e32 v227, v101, v105
	ds_read_b64_tr_b16 v[122:123], v207 offset:32768
	ds_read_b64_tr_b16 v[124:125], v207 offset:33792
	s_waitcnt lgkmcnt(10)
	v_mfma_f32_32x32x16_f16 v[50:65], v[114:117], v[154:157], v[34:49]
	v_cvt_pk_f16_f32 v160, v102, v103
	v_cvt_pk_f16_f32 v161, v104, v105
	v_add_f32_e32 v224, v106, v224
	v_add_f32_e32 v225, v107, v225
	v_add_f32_e32 v226, v108, v226
	v_add_f32_e32 v227, v109, v227
	ds_read_b64_tr_b16 v[118:119], v206 offset:34816
	ds_read_b64_tr_b16 v[120:121], v206 offset:35840
	s_waitcnt lgkmcnt(11)
	v_mfma_f32_32x32x16_f16 v[66:81], v[182:185], v[146:149], v[66:81]
	v_cvt_pk_f16_f32 v150, v106, v107
	v_cvt_pk_f16_f32 v151, v108, v109
	v_add_f32_e32 v224, v110, v224
	v_add_f32_e32 v225, v111, v225
	v_add_f32_e32 v226, v112, v226
	v_add_f32_e32 v227, v113, v227
	ds_read_b64_tr_b16 v[114:115], v207 offset:34816
	ds_read_b64_tr_b16 v[116:117], v207 offset:35840
	s_waitcnt lgkmcnt(12)
	v_mfma_f32_32x32x16_f16 v[50:65], v[174:177], v[146:149], v[50:65]
	v_cvt_pk_f16_f32 v152, v110, v111
	v_cvt_pk_f16_f32 v153, v112, v113
	v_add_f32_e32 v224, v82, v224
	v_add_f32_e32 v225, v83, v225
	v_add_f32_e32 v226, v84, v226
	v_add_f32_e32 v227, v85, v227
	ds_read_b64_tr_b16 v[106:107], v206 offset:36864
	ds_read_b64_tr_b16 v[108:109], v206 offset:37888
	s_waitcnt lgkmcnt(13)
	v_mfma_f32_32x32x16_f16 v[66:81], v[178:181], v[138:141], v[66:81]
	v_cvt_pk_f16_f32 v142, v82, v83
	v_cvt_pk_f16_f32 v143, v84, v85
	v_add_f32_e32 v224, v86, v224
	v_add_f32_e32 v225, v87, v225
	v_add_f32_e32 v226, v88, v226
	v_add_f32_e32 v227, v89, v227
	ds_read_b64_tr_b16 v[102:103], v207 offset:36864
	ds_read_b64_tr_b16 v[104:105], v207 offset:37888
	s_waitcnt lgkmcnt(14)
	v_mfma_f32_32x32x16_f16 v[50:65], v[166:169], v[138:141], v[50:65]
	v_cvt_pk_f16_f32 v144, v86, v87
	v_cvt_pk_f16_f32 v145, v88, v89
	v_add_f32_e32 v224, v90, v224
	v_add_f32_e32 v225, v91, v225
	v_add_f32_e32 v226, v92, v226
	v_add_f32_e32 v227, v93, v227
	ds_read_b64_tr_b16 v[98:99], v206 offset:38912
	ds_read_b64_tr_b16 v[100:101], v206 offset:39936
	s_waitcnt lgkmcnt(14)
	v_mfma_f32_32x32x16_f16 v[66:81], v[170:173], v[134:137], v[66:81]
	v_cvt_pk_f16_f32 v130, v90, v91
	v_cvt_pk_f16_f32 v131, v92, v93
	v_add_f32_e32 v224, v94, v224
	v_add_f32_e32 v225, v95, v225
	v_add_f32_e32 v226, v96, v226
	v_add_f32_e32 v227, v97, v227
	ds_read_b64_tr_b16 v[86:87], v207 offset:38912
	ds_read_b64_tr_b16 v[88:89], v207 offset:39936
	v_mfma_f32_32x32x16_f16 v[50:65], v[162:165], v[134:137], v[50:65]
	v_cvt_pk_f16_f32 v132, v94, v95
	v_cvt_pk_f16_f32 v133, v96, v97
	v_add_f32_e32 v224, v224, v225
	v_add_f32_e32 v226, v226, v227
	v_add_f32_e32 v84, v224, v226
	s_setprio 1
	s_add_u32 s54, s50, 0x2000
	s_addc_u32 s55, s51, 0
	s_add_i32 s26, s39, s36
	s_mov_b32 m0, s26
	s_nop 0
	global_load_lds_dwordx4 v221, s[54:55]
	v_max_f32_e32 v82, v66, v67
	s_nop 1
	v_max3_f32 v83, v68, v69, v51
	v_max3_f32 v82, v82, v50, v52
	v_max3_f32 v82, v82, v53, v70
	v_max3_f32 v83, v83, v72, v73
	v_max3_f32 v82, v82, v71, v54
	v_max3_f32 v83, v83, v56, v57
	v_max3_f32 v82, v82, v55, v74
	v_max3_f32 v83, v83, v76, v77
	v_max3_f32 v82, v82, v75, v58
	v_max3_f32 v83, v83, v60, v61
	v_max3_f32 v82, v82, v59, v78
	v_max3_f32 v83, v83, v80, v81
	v_max3_f32 v82, v82, v79, v62
	v_max3_f32 v83, v83, v64, v65
	v_max3_f32 v82, v82, v63, v83
	v_add_f32_e32 v183, v198, v84
	s_add_u32 s54, s52, 0x2000
	s_addc_u32 s55, s53, 0
	s_add_i32 s26, s43, s35
	s_mov_b32 m0, s26
	s_nop 0
	global_load_lds_dwordx4 v222, s[54:55]
	v_cmp_lt_f32_e32 vcc, s41, v82
	s_cmp_lg_u64 vcc, 0
	s_cselect_b64 s[26:27], -1, 0
	s_cbranch_vccnz .Lu0_12

.Lu1_1:
	ds_read_b64_tr_b16 v[178:179], v206 offset:40960
	ds_read_b64_tr_b16 v[180:181], v206 offset:41984
	s_waitcnt lgkmcnt(9)
	v_mfma_f32_32x32x16_f16 v[98:113], v[82:85], v[154:157], v[34:49]
	v_cvt_pk_f16_f32 v158, v66, v67
	v_cvt_pk_f16_f32 v159, v68, v69
	v_add_f32_e32 v224, v66, v70
	v_add_f32_e32 v225, v67, v71
	v_add_f32_e32 v226, v68, v72
	v_add_f32_e32 v227, v69, v73
	ds_read_b64_tr_b16 v[174:175], v207 offset:40960
	ds_read_b64_tr_b16 v[176:177], v207 offset:41984
	s_waitcnt lgkmcnt(10)
	v_mfma_f32_32x32x16_f16 v[82:97], v[170:173], v[154:157], v[34:49]
	v_cvt_pk_f16_f32 v160, v70, v71
	v_cvt_pk_f16_f32 v161, v72, v73
	v_add_f32_e32 v224, v74, v224
	v_add_f32_e32 v225, v75, v225
	v_add_f32_e32 v226, v76, v226
	v_add_f32_e32 v227, v77, v227
	ds_read_b64_tr_b16 v[170:171], v206 offset:43008
	ds_read_b64_tr_b16 v[172:173], v206 offset:44032
	s_waitcnt lgkmcnt(11)
	v_mfma_f32_32x32x16_f16 v[98:113], v[166:169], v[146:149], v[98:113]
	v_cvt_pk_f16_f32 v150, v74, v75
	v_cvt_pk_f16_f32 v151, v76, v77
	v_add_f32_e32 v224, v78, v224
	v_add_f32_e32 v225, v79, v225
	v_add_f32_e32 v226, v80, v226
	v_add_f32_e32 v227, v81, v227
	ds_read_b64_tr_b16 v[74:75], v207 offset:43008
	ds_read_b64_tr_b16 v[76:77], v207 offset:44032
	s_waitcnt lgkmcnt(12)
	v_mfma_f32_32x32x16_f16 v[82:97], v[162:165], v[146:149], v[82:97]
	v_cvt_pk_f16_f32 v152, v78, v79
	v_cvt_pk_f16_f32 v153, v80, v81
	v_add_f32_e32 v224, v50, v224
	v_add_f32_e32 v225, v51, v225
	v_add_f32_e32 v226, v52, v226
	v_add_f32_e32 v227, v53, v227
	ds_read_b64_tr_b16 v[70:71], v206 offset:45056
	ds_read_b64_tr_b16 v[72:73], v206 offset:46080
	s_waitcnt lgkmcnt(13)
	v_mfma_f32_32x32x16_f16 v[98:113], v[126:129], v[138:141], v[98:113]
	v_cvt_pk_f16_f32 v142, v50, v51
	v_cvt_pk_f16_f32 v143, v52, v53
	v_add_f32_e32 v224, v54, v224
	v_add_f32_e32 v225, v55, v225
	v_add_f32_e32 v226, v56, v226
	v_add_f32_e32 v227, v57, v227
	ds_read_b64_tr_b16 v[66:67], v207 offset:45056
	ds_read_b64_tr_b16 v[68:69], v207 offset:46080
	s_waitcnt lgkmcnt(14)
	v_mfma_f32_32x32x16_f16 v[82:97], v[122:125], v[138:141], v[82:97]
	v_cvt_pk_f16_f32 v144, v54, v55
	v_cvt_pk_f16_f32 v145, v56, v57
	v_add_f32_e32 v224, v58, v224
	v_add_f32_e32 v225, v59, v225
	v_add_f32_e32 v226, v60, v226
	v_add_f32_e32 v227, v61, v227
	ds_read_b64_tr_b16 v[54:55], v206 offset:47104
	ds_read_b64_tr_b16 v[56:57], v206 offset:48128
	s_waitcnt lgkmcnt(14)
	v_mfma_f32_32x32x16_f16 v[98:113], v[118:121], v[134:137], v[98:113]
	v_cvt_pk_f16_f32 v130, v58, v59
	v_cvt_pk_f16_f32 v131, v60, v61
	v_add_f32_e32 v224, v62, v224
	v_add_f32_e32 v225, v63, v225
	v_add_f32_e32 v226, v64, v226
	v_add_f32_e32 v227, v65, v227
	ds_read_b64_tr_b16 v[50:51], v207 offset:47104
	ds_read_b64_tr_b16 v[52:53], v207 offset:48128
	v_mfma_f32_32x32x16_f16 v[82:97], v[114:117], v[134:137], v[82:97]
	v_cvt_pk_f16_f32 v132, v62, v63
	v_cvt_pk_f16_f32 v133, v64, v65
	v_add_f32_e32 v224, v224, v225
	v_add_f32_e32 v226, v226, v227
	v_add_f32_e32 v60, v224, v226
	s_setprio 1
	s_add_i32 s26, s42, s36
	s_mov_b32 m0, s26
	s_nop 0
	global_load_lds_dwordx4 v221, s[50:51]
	s_add_i32 s26, s39, s35
	s_mov_b32 m0, s26
	s_nop 0
	global_load_lds_dwordx4 v222, s[52:53]
	v_max_f32_e32 v58, v98, v99
	v_max3_f32 v59, v100, v101, v83
	v_max3_f32 v58, v58, v82, v84
	v_max3_f32 v58, v58, v85, v102
	v_max3_f32 v59, v59, v104, v105
	v_max3_f32 v58, v58, v103, v86
	v_max3_f32 v59, v59, v88, v89
	v_max3_f32 v58, v58, v87, v106
	v_max3_f32 v59, v59, v108, v109
	v_max3_f32 v58, v58, v107, v90
	v_max3_f32 v59, v59, v92, v93
	v_max3_f32 v58, v58, v91, v110
	v_max3_f32 v59, v59, v112, v113
	v_max3_f32 v58, v58, v111, v94
	v_max3_f32 v59, v59, v96, v97
	v_max3_f32 v58, v58, v95, v59
	v_add_f32_e32 v198, v183, v60
	v_cmp_lt_f32_e32 vcc, s41, v58
	s_cmp_lg_u64 vcc, 0
	s_cselect_b64 s[26:27], -1, 0
	s_cbranch_vccnz .Lu1_9

.Lu1_4:
	s_add_i32 s26, s39, 0x2000
	s_cmpk_lg_i32 s39, 0x4000
	s_cselect_b32 s43, s26, 0
	ds_read_b64_tr_b16 v[126:127], v206 offset:24576
	ds_read_b64_tr_b16 v[128:129], v206 offset:25600
	s_waitcnt lgkmcnt(9)
	v_mfma_f32_32x32x16_f16 v[66:81], v[58:61], v[154:157], v[34:49]
	v_cvt_pk_f16_f32 v158, v98, v99
	v_cvt_pk_f16_f32 v159, v100, v101
	v_add_f32_e32 v224, v98, v102
	v_add_f32_e32 v225, v99, v103
	v_add_f32_e32 v226, v100, v104
	v_add_f32_e32 v227, v101, v105
	ds_read_b64_tr_b16 v[122:123], v207 offset:24576
	ds_read_b64_tr_b16 v[124:125], v207 offset:25600
	s_waitcnt lgkmcnt(10)
	v_mfma_f32_32x32x16_f16 v[50:65], v[114:117], v[154:157], v[34:49]
	v_cvt_pk_f16_f32 v160, v102, v103
	v_cvt_pk_f16_f32 v161, v104, v105
	v_add_f32_e32 v224, v106, v224
	v_add_f32_e32 v225, v107, v225
	v_add_f32_e32 v226, v108, v226
	v_add_f32_e32 v227, v109, v227
	ds_read_b64_tr_b16 v[118:119], v206 offset:26624
	ds_read_b64_tr_b16 v[120:121], v206 offset:27648
	s_waitcnt lgkmcnt(11)
	v_mfma_f32_32x32x16_f16 v[66:81], v[182:185], v[146:149], v[66:81]
	v_cvt_pk_f16_f32 v150, v106, v107
	v_cvt_pk_f16_f32 v151, v108, v109
	v_add_f32_e32 v224, v110, v224
	v_add_f32_e32 v225, v111, v225
	v_add_f32_e32 v226, v112, v226
	v_add_f32_e32 v227, v113, v227
	ds_read_b64_tr_b16 v[114:115], v207 offset:26624
	ds_read_b64_tr_b16 v[116:117], v207 offset:27648
	s_waitcnt lgkmcnt(12)
	v_mfma_f32_32x32x16_f16 v[50:65], v[174:177], v[146:149], v[50:65]
	v_cvt_pk_f16_f32 v152, v110, v111
	v_cvt_pk_f16_f32 v153, v112, v113
	v_add_f32_e32 v224, v82, v224
	v_add_f32_e32 v225, v83, v225
	v_add_f32_e32 v226, v84, v226
	v_add_f32_e32 v227, v85, v227
	ds_read_b64_tr_b16 v[106:107], v206 offset:28672
	ds_read_b64_tr_b16 v[108:109], v206 offset:29696
	s_waitcnt lgkmcnt(13)
	v_mfma_f32_32x32x16_f16 v[66:81], v[178:181], v[138:141], v[66:81]
	v_cvt_pk_f16_f32 v142, v82, v83
	v_cvt_pk_f16_f32 v143, v84, v85
	v_add_f32_e32 v224, v86, v224
	v_add_f32_e32 v225, v87, v225
	v_add_f32_e32 v226, v88, v226
	v_add_f32_e32 v227, v89, v227
	ds_read_b64_tr_b16 v[102:103], v207 offset:28672
	ds_read_b64_tr_b16 v[104:105], v207 offset:29696
	s_waitcnt lgkmcnt(14)
	v_mfma_f32_32x32x16_f16 v[50:65], v[166:169], v[138:141], v[50:65]
	v_cvt_pk_f16_f32 v144, v86, v87
	v_cvt_pk_f16_f32 v145, v88, v89
	v_add_f32_e32 v224, v90, v224
	v_add_f32_e32 v225, v91, v225
	v_add_f32_e32 v226, v92, v226
	v_add_f32_e32 v227, v93, v227
	ds_read_b64_tr_b16 v[98:99], v206 offset:30720
	ds_read_b64_tr_b16 v[100:101], v206 offset:31744
	s_waitcnt lgkmcnt(14)
	v_mfma_f32_32x32x16_f16 v[66:81], v[170:173], v[134:137], v[66:81]
	v_cvt_pk_f16_f32 v130, v90, v91
	v_cvt_pk_f16_f32 v131, v92, v93
	v_add_f32_e32 v224, v94, v224
	v_add_f32_e32 v225, v95, v225
	v_add_f32_e32 v226, v96, v226
	v_add_f32_e32 v227, v97, v227
	ds_read_b64_tr_b16 v[86:87], v207 offset:30720
	ds_read_b64_tr_b16 v[88:89], v207 offset:31744
	v_mfma_f32_32x32x16_f16 v[50:65], v[162:165], v[134:137], v[50:65]
	v_cvt_pk_f16_f32 v132, v94, v95
	v_cvt_pk_f16_f32 v133, v96, v97
	v_add_f32_e32 v224, v224, v225
	v_add_f32_e32 v226, v226, v227
	v_add_f32_e32 v84, v224, v226
	s_setprio 1
	s_add_u32 s54, s50, 0x2000
	s_addc_u32 s55, s51, 0
	s_add_i32 s26, s39, s36
	s_mov_b32 m0, s26
	s_nop 0
	global_load_lds_dwordx4 v221, s[54:55]
	v_max_f32_e32 v82, v66, v67
	s_nop 1
	v_max3_f32 v83, v68, v69, v51
	v_max3_f32 v82, v82, v50, v52
	v_max3_f32 v82, v82, v53, v70
	v_max3_f32 v83, v83, v72, v73
	v_max3_f32 v82, v82, v71, v54
	v_max3_f32 v83, v83, v56, v57
	v_max3_f32 v82, v82, v55, v74
	v_max3_f32 v83, v83, v76, v77
	v_max3_f32 v82, v82, v75, v58
	v_max3_f32 v83, v83, v60, v61
	v_max3_f32 v82, v82, v59, v78
	v_max3_f32 v83, v83, v80, v81
	v_max3_f32 v82, v82, v79, v62
	v_max3_f32 v83, v83, v64, v65
	v_max3_f32 v82, v82, v63, v83
	v_add_f32_e32 v183, v198, v84
	s_add_u32 s54, s52, 0x2000
	s_addc_u32 s55, s53, 0
	s_add_i32 s26, s43, s35
	s_mov_b32 m0, s26
	s_nop 0
	global_load_lds_dwordx4 v222, s[54:55]
	v_cmp_lt_f32_e32 vcc, s41, v82
	s_cmp_lg_u64 vcc, 0
	s_cselect_b64 s[26:27], -1, 0
	s_cbranch_vccnz .Lu1_12

.Lu2_1:
	ds_read_b64_tr_b16 v[178:179], v206 offset:32768
	ds_read_b64_tr_b16 v[180:181], v206 offset:33792
	s_waitcnt lgkmcnt(9)
	v_mfma_f32_32x32x16_f16 v[98:113], v[82:85], v[154:157], v[34:49]
	v_cvt_pk_f16_f32 v158, v66, v67
	v_cvt_pk_f16_f32 v159, v68, v69
	v_add_f32_e32 v224, v66, v70
	v_add_f32_e32 v225, v67, v71
	v_add_f32_e32 v226, v68, v72
	v_add_f32_e32 v227, v69, v73
	ds_read_b64_tr_b16 v[174:175], v207 offset:32768
	ds_read_b64_tr_b16 v[176:177], v207 offset:33792
	s_waitcnt lgkmcnt(10)
	v_mfma_f32_32x32x16_f16 v[82:97], v[170:173], v[154:157], v[34:49]
	v_cvt_pk_f16_f32 v160, v70, v71
	v_cvt_pk_f16_f32 v161, v72, v73
	v_add_f32_e32 v224, v74, v224
	v_add_f32_e32 v225, v75, v225
	v_add_f32_e32 v226, v76, v226
	v_add_f32_e32 v227, v77, v227
	ds_read_b64_tr_b16 v[170:171], v206 offset:34816
	ds_read_b64_tr_b16 v[172:173], v206 offset:35840
	s_waitcnt lgkmcnt(11)
	v_mfma_f32_32x32x16_f16 v[98:113], v[166:169], v[146:149], v[98:113]
	v_cvt_pk_f16_f32 v150, v74, v75
	v_cvt_pk_f16_f32 v151, v76, v77
	v_add_f32_e32 v224, v78, v224
	v_add_f32_e32 v225, v79, v225
	v_add_f32_e32 v226, v80, v226
	v_add_f32_e32 v227, v81, v227
	ds_read_b64_tr_b16 v[74:75], v207 offset:34816
	ds_read_b64_tr_b16 v[76:77], v207 offset:35840
	s_waitcnt lgkmcnt(12)
	v_mfma_f32_32x32x16_f16 v[82:97], v[162:165], v[146:149], v[82:97]
	v_cvt_pk_f16_f32 v152, v78, v79
	v_cvt_pk_f16_f32 v153, v80, v81
	v_add_f32_e32 v224, v50, v224
	v_add_f32_e32 v225, v51, v225
	v_add_f32_e32 v226, v52, v226
	v_add_f32_e32 v227, v53, v227
	ds_read_b64_tr_b16 v[70:71], v206 offset:36864
	ds_read_b64_tr_b16 v[72:73], v206 offset:37888
	s_waitcnt lgkmcnt(13)
	v_mfma_f32_32x32x16_f16 v[98:113], v[126:129], v[138:141], v[98:113]
	v_cvt_pk_f16_f32 v142, v50, v51
	v_cvt_pk_f16_f32 v143, v52, v53
	v_add_f32_e32 v224, v54, v224
	v_add_f32_e32 v225, v55, v225
	v_add_f32_e32 v226, v56, v226
	v_add_f32_e32 v227, v57, v227
	ds_read_b64_tr_b16 v[66:67], v207 offset:36864
	ds_read_b64_tr_b16 v[68:69], v207 offset:37888
	s_waitcnt lgkmcnt(14)
	v_mfma_f32_32x32x16_f16 v[82:97], v[122:125], v[138:141], v[82:97]
	v_cvt_pk_f16_f32 v144, v54, v55
	v_cvt_pk_f16_f32 v145, v56, v57
	v_add_f32_e32 v224, v58, v224
	v_add_f32_e32 v225, v59, v225
	v_add_f32_e32 v226, v60, v226
	v_add_f32_e32 v227, v61, v227
	ds_read_b64_tr_b16 v[54:55], v206 offset:38912
	ds_read_b64_tr_b16 v[56:57], v206 offset:39936
	s_waitcnt lgkmcnt(14)
	v_mfma_f32_32x32x16_f16 v[98:113], v[118:121], v[134:137], v[98:113]
	v_cvt_pk_f16_f32 v130, v58, v59
	v_cvt_pk_f16_f32 v131, v60, v61
	v_add_f32_e32 v224, v62, v224
	v_add_f32_e32 v225, v63, v225
	v_add_f32_e32 v226, v64, v226
	v_add_f32_e32 v227, v65, v227
	ds_read_b64_tr_b16 v[50:51], v207 offset:38912
	ds_read_b64_tr_b16 v[52:53], v207 offset:39936
	v_mfma_f32_32x32x16_f16 v[82:97], v[114:117], v[134:137], v[82:97]
	v_cvt_pk_f16_f32 v132, v62, v63
	v_cvt_pk_f16_f32 v133, v64, v65
	v_add_f32_e32 v224, v224, v225
	v_add_f32_e32 v226, v226, v227
	v_add_f32_e32 v60, v224, v226
	s_setprio 1
	s_add_i32 s26, s42, s36
	s_mov_b32 m0, s26
	s_nop 0
	global_load_lds_dwordx4 v221, s[50:51]
	s_add_i32 s26, s39, s35
	s_mov_b32 m0, s26
	s_nop 0
	global_load_lds_dwordx4 v222, s[52:53]
	v_max_f32_e32 v58, v98, v99
	v_max3_f32 v59, v100, v101, v83
	v_max3_f32 v58, v58, v82, v84
	v_max3_f32 v58, v58, v85, v102
	v_max3_f32 v59, v59, v104, v105
	v_max3_f32 v58, v58, v103, v86
	v_max3_f32 v59, v59, v88, v89
	v_max3_f32 v58, v58, v87, v106
	v_max3_f32 v59, v59, v108, v109
	v_max3_f32 v58, v58, v107, v90
	v_max3_f32 v59, v59, v92, v93
	v_max3_f32 v58, v58, v91, v110
	v_max3_f32 v59, v59, v112, v113
	v_max3_f32 v58, v58, v111, v94
	v_max3_f32 v59, v59, v96, v97
	v_max3_f32 v58, v58, v95, v59
	v_add_f32_e32 v198, v183, v60
	v_cmp_lt_f32_e32 vcc, s41, v58
	s_cmp_lg_u64 vcc, 0
	s_cselect_b64 s[26:27], -1, 0
	s_cbranch_vccnz .Lu2_9

.Lu2_4:
	s_add_i32 s26, s39, 0x2000
	s_cmpk_lg_i32 s39, 0x4000
	s_cselect_b32 s43, s26, 0
	ds_read_b64_tr_b16 v[126:127], v206 offset:40960
	ds_read_b64_tr_b16 v[128:129], v206 offset:41984
	s_waitcnt lgkmcnt(9)
	v_mfma_f32_32x32x16_f16 v[66:81], v[58:61], v[154:157], v[34:49]
	v_cvt_pk_f16_f32 v158, v98, v99
	v_cvt_pk_f16_f32 v159, v100, v101
	v_add_f32_e32 v224, v98, v102
	v_add_f32_e32 v225, v99, v103
	v_add_f32_e32 v226, v100, v104
	v_add_f32_e32 v227, v101, v105
	ds_read_b64_tr_b16 v[122:123], v207 offset:40960
	ds_read_b64_tr_b16 v[124:125], v207 offset:41984
	s_waitcnt lgkmcnt(10)
	v_mfma_f32_32x32x16_f16 v[50:65], v[114:117], v[154:157], v[34:49]
	v_cvt_pk_f16_f32 v160, v102, v103
	v_cvt_pk_f16_f32 v161, v104, v105
	v_add_f32_e32 v224, v106, v224
	v_add_f32_e32 v225, v107, v225
	v_add_f32_e32 v226, v108, v226
	v_add_f32_e32 v227, v109, v227
	ds_read_b64_tr_b16 v[118:119], v206 offset:43008
	ds_read_b64_tr_b16 v[120:121], v206 offset:44032
	s_waitcnt lgkmcnt(11)
	v_mfma_f32_32x32x16_f16 v[66:81], v[182:185], v[146:149], v[66:81]
	v_cvt_pk_f16_f32 v150, v106, v107
	v_cvt_pk_f16_f32 v151, v108, v109
	v_add_f32_e32 v224, v110, v224
	v_add_f32_e32 v225, v111, v225
	v_add_f32_e32 v226, v112, v226
	v_add_f32_e32 v227, v113, v227
	ds_read_b64_tr_b16 v[114:115], v207 offset:43008
	ds_read_b64_tr_b16 v[116:117], v207 offset:44032
	s_waitcnt lgkmcnt(12)
	v_mfma_f32_32x32x16_f16 v[50:65], v[174:177], v[146:149], v[50:65]
	v_cvt_pk_f16_f32 v152, v110, v111
	v_cvt_pk_f16_f32 v153, v112, v113
	v_add_f32_e32 v224, v82, v224
	v_add_f32_e32 v225, v83, v225
	v_add_f32_e32 v226, v84, v226
	v_add_f32_e32 v227, v85, v227
	ds_read_b64_tr_b16 v[106:107], v206 offset:45056
	ds_read_b64_tr_b16 v[108:109], v206 offset:46080
	s_waitcnt lgkmcnt(13)
	v_mfma_f32_32x32x16_f16 v[66:81], v[178:181], v[138:141], v[66:81]
	v_cvt_pk_f16_f32 v142, v82, v83
	v_cvt_pk_f16_f32 v143, v84, v85
	v_add_f32_e32 v224, v86, v224
	v_add_f32_e32 v225, v87, v225
	v_add_f32_e32 v226, v88, v226
	v_add_f32_e32 v227, v89, v227
	ds_read_b64_tr_b16 v[102:103], v207 offset:45056
	ds_read_b64_tr_b16 v[104:105], v207 offset:46080
	s_waitcnt lgkmcnt(14)
	v_mfma_f32_32x32x16_f16 v[50:65], v[166:169], v[138:141], v[50:65]
	v_cvt_pk_f16_f32 v144, v86, v87
	v_cvt_pk_f16_f32 v145, v88, v89
	v_add_f32_e32 v224, v90, v224
	v_add_f32_e32 v225, v91, v225
	v_add_f32_e32 v226, v92, v226
	v_add_f32_e32 v227, v93, v227
	ds_read_b64_tr_b16 v[98:99], v206 offset:47104
	ds_read_b64_tr_b16 v[100:101], v206 offset:48128
	s_waitcnt lgkmcnt(14)
	v_mfma_f32_32x32x16_f16 v[66:81], v[170:173], v[134:137], v[66:81]
	v_cvt_pk_f16_f32 v130, v90, v91
	v_cvt_pk_f16_f32 v131, v92, v93
	v_add_f32_e32 v224, v94, v224
	v_add_f32_e32 v225, v95, v225
	v_add_f32_e32 v226, v96, v226
	v_add_f32_e32 v227, v97, v227
	ds_read_b64_tr_b16 v[86:87], v207 offset:47104
	ds_read_b64_tr_b16 v[88:89], v207 offset:48128
	v_mfma_f32_32x32x16_f16 v[50:65], v[162:165], v[134:137], v[50:65]
	v_cvt_pk_f16_f32 v132, v94, v95
	v_cvt_pk_f16_f32 v133, v96, v97
	v_add_f32_e32 v224, v224, v225
	v_add_f32_e32 v226, v226, v227
	v_add_f32_e32 v84, v224, v226
	s_setprio 1
	s_add_u32 s54, s50, 0x2000
	s_addc_u32 s55, s51, 0
	s_add_i32 s26, s39, s36
	s_mov_b32 m0, s26
	s_nop 0
	global_load_lds_dwordx4 v221, s[54:55]
	v_max_f32_e32 v82, v66, v67
	s_nop 1
	v_max3_f32 v83, v68, v69, v51
	v_max3_f32 v82, v82, v50, v52
	v_max3_f32 v82, v82, v53, v70
	v_max3_f32 v83, v83, v72, v73
	v_max3_f32 v82, v82, v71, v54
	v_max3_f32 v83, v83, v56, v57
	v_max3_f32 v82, v82, v55, v74
	v_max3_f32 v83, v83, v76, v77
	v_max3_f32 v82, v82, v75, v58
	v_max3_f32 v83, v83, v60, v61
	v_max3_f32 v82, v82, v59, v78
	v_max3_f32 v83, v83, v80, v81
	v_max3_f32 v82, v82, v79, v62
	v_max3_f32 v83, v83, v64, v65
	v_max3_f32 v82, v82, v63, v83
	v_add_f32_e32 v183, v198, v84
	s_add_u32 s54, s52, 0x2000
	s_addc_u32 s55, s53, 0
	s_add_i32 s26, s43, s35
	s_mov_b32 m0, s26
	s_nop 0
	global_load_lds_dwordx4 v222, s[54:55]
	v_cmp_lt_f32_e32 vcc, s41, v82
	s_cmp_lg_u64 vcc, 0
	s_cselect_b64 s[26:27], -1, 0
	s_cbranch_vccnz .Lu2_12
